# router LDS read pipelining + norm1 layer-1 first expert pair requested before the row arithmetic and accumulated after the stores
# speedup vs baseline: 1.0076x; 1.0076x over previous
; __device__ __forceinline__ void gather_y(const Ctx& F, const int s, f32x4 (&acc)[8]) {
; #pragma unroll
;     for (int j = 0; j < 8; ++j) acc[j] = (f32x4){0.f, 0.f, 0.f, 0.f};
;     unsigned m = (unsigned)__ballot(s >= 0) & 0xffffu;
;     while (m) {
;         const int e0 = __builtin_ctz(m); m &= m - 1;
;         const bool two = m != 0; const int e1 = two ? __builtin_ctz(m) : e0; if (two) m &= m - 1;
;         const int s0 = __builtin_amdgcn_readlane(s, e0), s1 = __builtin_amdgcn_readlane(s, e1);
;         const unsigned char* y0 = F.y8 + (size_t)s0 * DM + 4 * F.lane; const unsigned char* y1 = F.y8 + (size_t)s1 * DM + 4 * F.lane;
;         unsigned w0[8], w1[8];
; #pragma unroll
;         for (int j = 0; j < 8; ++j) w0[j] = __builtin_nontemporal_load((const unsigned*)(y0 + 256 * j));
; #pragma unroll
;         for (int j = 0; j < 8; ++j) w1[j] = __builtin_nontemporal_load((const unsigned*)(y1 + 256 * j));
; __device__ __forceinline__ void phase_norm1(const Params& p, const Ctx& F, const int l) {
;     ...
;     for (; t < TPB; t += tstride) {
;         const bool isctx = t < CTXL;
;         const int mrow = isctx ? 8 : b;
;         const float* xs; float* xd; row_ptrs(p, F, l, b, t, xs, xd);
;         f32x4 v[8];
; #pragma unroll
;         for (int j = 0; j < 8; ++j) v[j] = vn[j] + (f32x4){bflo(dn[j].x), bfhi(dn[j].x), bflo(dn[j].y), bfhi(dn[j].y)};
;         if (comb) {
;             const float* gt = F.mod + (size_t)((l - 1) * 9 + mrow) * MODW + 5 * DM;
; #pragma unroll
;             for (int j = 0; j < 8; ++j) { v[j] += *((const f32x4*)gt + F.lane + 64 * j) * accn[j] * (1.f / Y_SCALE); if (!fin) *((f32x4*)xd + F.lane + 64 * j) = v[j]; }
;         }
;         { const int t2 = t + tstride;
;           if (t2 < TPB) { const float* xs2; float* xd2; row_ptrs(p, F, l, b, t2, xs2, xd2);
; #pragma unroll
;             for (int j = 0; j < 8; ++j) vn[j] = __builtin_nontemporal_load((const f32x4*)xs2 + F.lane + 64 * j);
;             if (comb) {
; #pragma unroll
;                 for (int j = 0; j < 8; ++j) dn[j] = __builtin_nontemporal_load((const u32x2*)(F.dlt + ((size_t)b * TPB + t2) * DM + 4 * F.lane + 256 * j)); }
;             if (comb) { { if (fin) gather_y1(F, sn, accn); else gather_y(F, sn, accn); } const int t3 = t2 + tstride; sn = -1; if (t3 < TPB && F.lane < 16) sn = F.slot[(unsigned)((b * 16 + F.lane) * TPB + t3)]; } } }
.LBB0_151:
	v_and_b32_e32 v1, 64, v197
	v_add_u32_e32 v1, 64, v1
	v_xor_b32_e32 v69, 1, v197
	v_cmp_lt_i32_e32 vcc, v69, v1
	s_mul_i32 s22, s78, 9
	s_lshl_b32 s60, s78, 11
	v_cndmask_b32_e32 v69, v197, v69, vcc
	v_lshlrev_b32_e32 v203, 2, v69
	v_xor_b32_e32 v69, 2, v197
	v_cmp_lt_i32_e32 vcc, v69, v1
	v_readlane_b32 s36, v252, 37
	s_add_i32 s23, s22, -9
	v_cndmask_b32_e32 v69, v197, v69, vcc
	v_lshlrev_b32_e32 v204, 2, v69
	v_xor_b32_e32 v69, 4, v197
	v_cmp_lt_i32_e32 vcc, v69, v1
	s_lshl_b64 s[0:1], s[60:61], 2
	v_readlane_b32 s48, v252, 49
	v_cndmask_b32_e32 v69, v197, v69, vcc
	v_lshlrev_b32_e32 v205, 2, v69
	v_xor_b32_e32 v69, 8, v197
	v_cmp_lt_i32_e32 vcc, v69, v1
	v_readlane_b32 s49, v252, 50
	s_add_u32 s0, s48, s0
	v_cndmask_b32_e32 v69, v197, v69, vcc
	s_addc_u32 s1, s49, s1
	v_lshlrev_b32_e32 v206, 2, v69
	v_xor_b32_e32 v69, 16, v197
	s_add_u32 s24, s2, 0x100000
	v_cmp_lt_i32_e32 vcc, v69, v1
	s_addc_u32 s25, s3, 0
	s_add_u32 s10, s2, 0xa00000
	v_cndmask_b32_e32 v69, v197, v69, vcc
	v_lshlrev_b32_e32 v207, 2, v69
	v_xor_b32_e32 v69, 32, v197
	v_lshl_add_u64 v[186:187], s[0:1], 0, v[34:35]
	s_mov_b64 s[0:1], 0x1000
	s_addc_u32 s11, s3, 0
	v_cmp_lt_i32_e32 vcc, v69, v1
	v_lshl_add_u64 v[188:189], v[186:187], 0, s[0:1]
	s_mov_b64 s[0:1], 0x1400
	s_add_u32 s26, s2, 0x900000
	v_cndmask_b32_e32 v1, v197, v69, vcc
	v_mov_b32_e32 v69, v35
	v_lshl_add_u64 v[190:191], v[186:187], 0, s[0:1]
	s_mov_b64 s[0:1], 0x1800
	s_addc_u32 s27, s3, 0
	v_lshlrev_b32_e32 v208, 2, v1
	v_lshl_add_u64 v[68:69], s[2:3], 0, v[68:69]
	s_mov_b64 s[2:3], 0x28e00000
	v_lshl_add_u32 v1, s19, 4, v72
	v_lshl_add_u64 v[192:193], v[186:187], 0, s[0:1]
	s_mov_b64 s[0:1], 0x1c00
	s_lshl_b32 s28, s19, 12
	s_lshl_b32 s29, s19, 8
	s_mov_b32 s34, -1
	v_lshl_add_u64 v[180:181], v[68:69], 0, s[2:3]
	v_cmp_eq_u32_e64 s[6:7], 0, v72
	v_lshl_add_u64 v[182:183], v[70:71], 1, s[12:13]
	s_waitcnt vmcnt(0)
	v_mov_b32_e32 v251, v202
	v_lshl_add_u64 v[184:185], s[4:5], 0, v[70:71]
	v_cmp_gt_u32_e64 s[4:5], 16, v72
	v_mul_u32_u24_e32 v209, 0x1100, v1
	v_lshl_add_u64 v[194:195], v[186:187], 0, s[0:1]
	v_readlane_b32 s37, v252, 38
	v_readlane_b32 s38, v252, 39
	v_readlane_b32 s39, v252, 40
	v_readlane_b32 s40, v252, 41
	v_readlane_b32 s41, v252, 42
	v_readlane_b32 s42, v252, 43
	v_readlane_b32 s43, v252, 44
	v_readlane_b32 s44, v252, 45
	v_readlane_b32 s45, v252, 46
	v_readlane_b32 s46, v252, 47
	v_readlane_b32 s47, v252, 48
	v_readlane_b32 s50, v252, 51
	v_readlane_b32 s51, v252, 52
	s_branch .LBB0_153
.LBB0_152:
	s_or_b64 exec, exec, s[0:1]
	s_cmp_lt_u32 s57, 2
	s_cbranch_scc1 .Lgs_g1done
	s_waitcnt vmcnt(0)
	v_cvt_pk_f32_fp8_e32 v[200:201], v234
	v_cvt_pk_f32_fp8_sdwa v[212:213], v234 src0_sel:WORD_1
	v_pk_add_f32 v[2:3], v[2:3], v[200:201]
	v_pk_add_f32 v[4:5], v[4:5], v[212:213]
	v_cvt_pk_f32_fp8_e32 v[200:201], v242
	v_cvt_pk_f32_fp8_sdwa v[212:213], v242 src0_sel:WORD_1
	v_pk_fma_f32 v[2:3], s[58:59], v[200:201], v[2:3] op_sel_hi:[0,1,1]
	v_pk_fma_f32 v[4:5], s[58:59], v[212:213], v[4:5] op_sel_hi:[0,1,1]
	v_cvt_pk_f32_fp8_e32 v[200:201], v235
	v_cvt_pk_f32_fp8_sdwa v[212:213], v235 src0_sel:WORD_1
	v_pk_add_f32 v[6:7], v[6:7], v[200:201]
	v_pk_add_f32 v[8:9], v[8:9], v[212:213]
	v_cvt_pk_f32_fp8_e32 v[200:201], v243
	v_cvt_pk_f32_fp8_sdwa v[212:213], v243 src0_sel:WORD_1
	v_pk_fma_f32 v[6:7], s[58:59], v[200:201], v[6:7] op_sel_hi:[0,1,1]
	v_pk_fma_f32 v[8:9], s[58:59], v[212:213], v[8:9] op_sel_hi:[0,1,1]
	v_cvt_pk_f32_fp8_e32 v[200:201], v236
	v_cvt_pk_f32_fp8_sdwa v[212:213], v236 src0_sel:WORD_1
	v_pk_add_f32 v[10:11], v[10:11], v[200:201]
	v_pk_add_f32 v[12:13], v[12:13], v[212:213]
	v_cvt_pk_f32_fp8_e32 v[200:201], v244
	v_cvt_pk_f32_fp8_sdwa v[212:213], v244 src0_sel:WORD_1
	v_pk_fma_f32 v[10:11], s[58:59], v[200:201], v[10:11] op_sel_hi:[0,1,1]
	v_pk_fma_f32 v[12:13], s[58:59], v[212:213], v[12:13] op_sel_hi:[0,1,1]
	v_cvt_pk_f32_fp8_e32 v[200:201], v237
	v_cvt_pk_f32_fp8_sdwa v[212:213], v237 src0_sel:WORD_1
	v_pk_add_f32 v[14:15], v[14:15], v[200:201]
	v_pk_add_f32 v[16:17], v[16:17], v[212:213]
	v_cvt_pk_f32_fp8_e32 v[200:201], v245
	v_cvt_pk_f32_fp8_sdwa v[212:213], v245 src0_sel:WORD_1
	v_pk_fma_f32 v[14:15], s[58:59], v[200:201], v[14:15] op_sel_hi:[0,1,1]
	v_pk_fma_f32 v[16:17], s[58:59], v[212:213], v[16:17] op_sel_hi:[0,1,1]
	v_cvt_pk_f32_fp8_e32 v[200:201], v238
	v_cvt_pk_f32_fp8_sdwa v[212:213], v238 src0_sel:WORD_1
	v_pk_add_f32 v[18:19], v[18:19], v[200:201]
	v_pk_add_f32 v[20:21], v[20:21], v[212:213]
	v_cvt_pk_f32_fp8_e32 v[200:201], v246
	v_cvt_pk_f32_fp8_sdwa v[212:213], v246 src0_sel:WORD_1
	v_pk_fma_f32 v[18:19], s[58:59], v[200:201], v[18:19] op_sel_hi:[0,1,1]
	v_pk_fma_f32 v[20:21], s[58:59], v[212:213], v[20:21] op_sel_hi:[0,1,1]
	v_cvt_pk_f32_fp8_e32 v[200:201], v239
	v_cvt_pk_f32_fp8_sdwa v[212:213], v239 src0_sel:WORD_1
	v_pk_add_f32 v[22:23], v[22:23], v[200:201]
	v_pk_add_f32 v[24:25], v[24:25], v[212:213]
	v_cvt_pk_f32_fp8_e32 v[200:201], v247
	v_cvt_pk_f32_fp8_sdwa v[212:213], v247 src0_sel:WORD_1
	v_pk_fma_f32 v[22:23], s[58:59], v[200:201], v[22:23] op_sel_hi:[0,1,1]
	v_pk_fma_f32 v[24:25], s[58:59], v[212:213], v[24:25] op_sel_hi:[0,1,1]
	v_cvt_pk_f32_fp8_e32 v[200:201], v240
	v_cvt_pk_f32_fp8_sdwa v[212:213], v240 src0_sel:WORD_1
	v_pk_add_f32 v[26:27], v[26:27], v[200:201]
	v_pk_add_f32 v[28:29], v[28:29], v[212:213]
	v_cvt_pk_f32_fp8_e32 v[200:201], v248
	v_cvt_pk_f32_fp8_sdwa v[212:213], v248 src0_sel:WORD_1
	v_pk_fma_f32 v[26:27], s[58:59], v[200:201], v[26:27] op_sel_hi:[0,1,1]
	v_pk_fma_f32 v[28:29], s[58:59], v[212:213], v[28:29] op_sel_hi:[0,1,1]
	v_cvt_pk_f32_fp8_e32 v[200:201], v241
	v_cvt_pk_f32_fp8_sdwa v[212:213], v241 src0_sel:WORD_1
	v_pk_add_f32 v[30:31], v[30:31], v[200:201]
	v_pk_add_f32 v[32:33], v[32:33], v[212:213]
	v_cvt_pk_f32_fp8_e32 v[200:201], v249
	v_cvt_pk_f32_fp8_sdwa v[212:213], v249 src0_sel:WORD_1
	v_pk_fma_f32 v[30:31], s[58:59], v[200:201], v[30:31] op_sel_hi:[0,1,1]
	v_pk_fma_f32 v[32:33], s[58:59], v[212:213], v[32:33] op_sel_hi:[0,1,1]
	s_mov_b32 s0, s56
	s_cmp_lg_u32 s0, 0
	s_cbranch_scc0 .Lgs_g1done

; __device__ __forceinline__ float bflo(unsigned w) { return __uint_as_float(w << 16); }
; __device__ __forceinline__ float bfhi(unsigned w) { return __uint_as_float(w & 0xffff0000u); }
; __device__ __forceinline__ void phase_norm1(const Params& p, const Ctx& F, const int l) {
;     ...
;     for (; t < TPB; t += tstride) {
;         const bool isctx = t < CTXL;
;         const int mrow = isctx ? 8 : b;
;         const float* xs; float* xd; row_ptrs(p, F, l, b, t, xs, xd);
;         f32x4 v[8];
; #pragma unroll
;         for (int j = 0; j < 8; ++j) v[j] = vn[j] + (f32x4){bflo(dn[j].x), bfhi(dn[j].x), bflo(dn[j].y), bfhi(dn[j].y)};
;         if (comb) {
;             const float* gt = F.mod + (size_t)((l - 1) * 9 + mrow) * MODW + 5 * DM;
; #pragma unroll
;             for (int j = 0; j < 8; ++j) { v[j] += *((const f32x4*)gt + F.lane + 64 * j) * accn[j] * (1.f / Y_SCALE); if (!fin) *((f32x4*)xd + F.lane + 64 * j) = v[j]; }
;         }
;         { const int t2 = t + tstride;
;           if (t2 < TPB) { const float* xs2; float* xd2; row_ptrs(p, F, l, b, t2, xs2, xd2);
; #pragma unroll
;             for (int j = 0; j < 8; ++j) vn[j] = __builtin_nontemporal_load((const f32x4*)xs2 + F.lane + 64 * j);
;             if (comb) {
; #pragma unroll
;                 for (int j = 0; j < 8; ++j) dn[j] = __builtin_nontemporal_load((const u32x2*)(F.dlt + ((size_t)b * TPB + t2) * DM + 4 * F.lane + 256 * j)); }
;             if (comb) { { if (fin) gather_y1(F, sn, accn); else gather_y(F, sn, accn); } const int t3 = t2 + tstride; sn = -1; if (t3 < TPB && F.lane < 16) sn = F.slot[(unsigned)((b * 16 + F.lane) * TPB + t3)]; } } }
;         if (mrow != cur_m) { cur_m = mrow;
.Lgs_g1done:
	s_andn2_b64 vcc, exec, s[2:3]
	s_mov_b32 s34, s30
	s_mov_b32 s20, s31
	s_cbranch_vccz .LBB0_176

; __device__ __forceinline__ float bflo(unsigned w) { return __uint_as_float(w << 16); }
; __device__ __forceinline__ float bfhi(unsigned w) { return __uint_as_float(w & 0xffff0000u); }
; __device__ __forceinline__ void phase_norm1(const Params& p, const Ctx& F, const int l) {
;     ...
;         const bool isctx = t < CTXL;
;         const int mrow = isctx ? 8 : b;
;         const float* xs; float* xd; row_ptrs(p, F, l, b, t, xs, xd);
;         f32x4 v[8];
; #pragma unroll
;         for (int j = 0; j < 8; ++j) v[j] = vn[j] + (f32x4){bflo(dn[j].x), bfhi(dn[j].x), bflo(dn[j].y), bfhi(dn[j].y)};
;         if (comb) {
;             const float* gt = F.mod + (size_t)((l - 1) * 9 + mrow) * MODW + 5 * DM;
; #pragma unroll
;             for (int j = 0; j < 8; ++j) { v[j] += *((const f32x4*)gt + F.lane + 64 * j) * accn[j] * (1.f / Y_SCALE); if (!fin) *((f32x4*)xd + F.lane + 64 * j) = v[j]; }
;         }
.LBB0_157:
	v_readlane_b32 s14, v254, 31
	v_readlane_b32 s15, v254, 32
	s_and_b64 s[0:1], s[0:1], exec
	s_waitcnt vmcnt(0)
	v_mov_b32_e32 v202, v251
	s_mov_b32 s57, 0
	v_lshlrev_b32_e32 v132, 16, v164
	v_and_b32_e32 v133, 0xffff0000, v164
	v_lshlrev_b32_e32 v134, 16, v165
	v_and_b32_e32 v135, 0xffff0000, v165
	v_lshlrev_b32_e32 v136, 16, v166
	v_and_b32_e32 v137, 0xffff0000, v166
	v_lshlrev_b32_e32 v138, 16, v167
	v_and_b32_e32 v139, 0xffff0000, v167
	v_lshlrev_b32_e32 v140, 16, v168
	v_and_b32_e32 v141, 0xffff0000, v168
	v_lshlrev_b32_e32 v142, 16, v169
	v_and_b32_e32 v143, 0xffff0000, v169
	v_lshlrev_b32_e32 v144, 16, v170
	v_and_b32_e32 v145, 0xffff0000, v170
	v_lshlrev_b32_e32 v146, 16, v171
	v_and_b32_e32 v147, 0xffff0000, v171
	v_lshlrev_b32_e32 v148, 16, v172
	v_and_b32_e32 v149, 0xffff0000, v172
	v_lshlrev_b32_e32 v150, 16, v173
	v_and_b32_e32 v151, 0xffff0000, v173
	v_lshlrev_b32_e32 v152, 16, v176
	v_and_b32_e32 v153, 0xffff0000, v176
	v_lshlrev_b32_e32 v154, 16, v177
	v_and_b32_e32 v155, 0xffff0000, v177
	v_lshlrev_b32_e32 v156, 16, v178
	v_and_b32_e32 v157, 0xffff0000, v178
	v_lshlrev_b32_e32 v158, 16, v179
	v_and_b32_e32 v159, 0xffff0000, v179
	v_lshlrev_b32_e32 v160, 16, v174
	v_and_b32_e32 v161, 0xffff0000, v174
	v_lshlrev_b32_e32 v162, 16, v175
	v_and_b32_e32 v163, 0xffff0000, v175
	v_cndmask_b32_e64 v1, 0, 1, s[14:15]
	s_cselect_b32 s30, 8, s19
	v_pk_add_f32 v[134:135], v[38:39], v[134:135]
	v_pk_add_f32 v[132:133], v[36:37], v[132:133]
	v_pk_add_f32 v[138:139], v[42:43], v[138:139]
	v_pk_add_f32 v[136:137], v[40:41], v[136:137]
	v_pk_add_f32 v[142:143], v[46:47], v[142:143]
	v_pk_add_f32 v[140:141], v[44:45], v[140:141]
	v_pk_add_f32 v[146:147], v[50:51], v[146:147]
	v_pk_add_f32 v[144:145], v[48:49], v[144:145]
	v_pk_add_f32 v[150:151], v[54:55], v[150:151]
	v_pk_add_f32 v[148:149], v[52:53], v[148:149]
	v_pk_add_f32 v[154:155], v[58:59], v[154:155]
	v_pk_add_f32 v[152:153], v[56:57], v[152:153]
	v_pk_add_f32 v[158:159], v[62:63], v[158:159]
	v_pk_add_f32 v[156:157], v[60:61], v[156:157]
	v_pk_add_f32 v[162:163], v[66:67], v[162:163]
	v_cmp_ne_u32_e64 s[0:1], 1, v1
	s_andn2_b64 vcc, exec, s[14:15]
	v_pk_add_f32 v[160:161], v[64:65], v[160:161]
	s_cbranch_vccnz .LBB0_159
	s_lshl_b64 s[2:3], s[2:3], 13
	s_add_u32 s2, s12, s2
	s_addc_u32 s3, s13, s3
	s_add_i32 s12, s23, s30
	s_mul_hi_u32 s13, s12, 0xc000
	s_mul_i32 s12, s12, 0xc000
	s_add_u32 s12, s24, s12
	s_addc_u32 s13, s25, s13
	v_lshl_add_u64 v[198:199], s[12:13], 0, v[34:35]
	s_mov_b32 s12, 0xb000
	v_add_co_u32_e32 v200, vcc, s12, v198
	s_mov_b64 s[12:13], 0xa000
	s_nop 0
	v_addc_co_u32_e32 v201, vcc, 0, v199, vcc
	v_lshl_add_u64 v[198:199], v[198:199], 0, s[12:13]
	global_load_dwordx4 v[210:213], v[200:201], off offset:-4096
	global_load_dwordx4 v[224:227], v[198:199], off offset:1024
	global_load_dwordx4 v[228:231], v[198:199], off offset:2048
	global_load_dwordx4 v[232:235], v[198:199], off offset:3072
	global_load_dwordx4 v[236:239], v[200:201], off
	global_load_dwordx4 v[240:243], v[200:201], off offset:1024
	global_load_dwordx4 v[244:247], v[200:201], off offset:2048
	global_load_dwordx4 v[248:251], v[200:201], off offset:3072
	s_mov_b32 s12, 0x3d000000
	s_waitcnt vmcnt(0)
	v_pk_mul_f32 v[212:213], v[4:5], v[212:213]
	v_pk_mul_f32 v[210:211], v[2:3], v[210:211]
	v_pk_fma_f32 v[134:135], v[212:213], s[12:13], v[134:135] op_sel_hi:[1,0,1]
	v_pk_fma_f32 v[132:133], v[210:211], s[12:13], v[132:133] op_sel_hi:[1,0,1]
	global_store_dwordx4 v34, v[132:135], s[2:3]
	v_pk_mul_f32 v[226:227], v[8:9], v[226:227]
	v_pk_mul_f32 v[224:225], v[6:7], v[224:225]
	v_pk_fma_f32 v[138:139], v[226:227], s[12:13], v[138:139] op_sel_hi:[1,0,1]
	v_pk_fma_f32 v[136:137], v[224:225], s[12:13], v[136:137] op_sel_hi:[1,0,1]
	global_store_dwordx4 v34, v[136:139], s[2:3] offset:1024
	v_pk_mul_f32 v[230:231], v[12:13], v[230:231]
	v_pk_mul_f32 v[228:229], v[10:11], v[228:229]
	v_pk_fma_f32 v[142:143], v[230:231], s[12:13], v[142:143] op_sel_hi:[1,0,1]
	v_pk_fma_f32 v[140:141], v[228:229], s[12:13], v[140:141] op_sel_hi:[1,0,1]
	global_store_dwordx4 v34, v[140:143], s[2:3] offset:2048
	v_pk_mul_f32 v[234:235], v[16:17], v[234:235]
	v_pk_mul_f32 v[232:233], v[14:15], v[232:233]
	v_pk_fma_f32 v[146:147], v[234:235], s[12:13], v[146:147] op_sel_hi:[1,0,1]
	v_pk_fma_f32 v[144:145], v[232:233], s[12:13], v[144:145] op_sel_hi:[1,0,1]
	global_store_dwordx4 v34, v[144:147], s[2:3] offset:3072
	v_lshl_add_u64 v[198:199], s[2:3], 0, v[34:35]
	v_add_co_u32_e32 v198, vcc, 0x1000, v198
	s_nop 1
	v_addc_co_u32_e32 v199, vcc, 0, v199, vcc
	v_pk_mul_f32 v[238:239], v[20:21], v[238:239]
	v_pk_mul_f32 v[236:237], v[18:19], v[236:237]
	v_pk_fma_f32 v[150:151], v[238:239], s[12:13], v[150:151] op_sel_hi:[1,0,1]
	v_pk_fma_f32 v[148:149], v[236:237], s[12:13], v[148:149] op_sel_hi:[1,0,1]
	global_store_dwordx4 v[198:199], v[148:151], off
	v_pk_mul_f32 v[242:243], v[24:25], v[242:243]
	v_pk_mul_f32 v[240:241], v[22:23], v[240:241]
	v_pk_fma_f32 v[154:155], v[242:243], s[12:13], v[154:155] op_sel_hi:[1,0,1]
	v_pk_fma_f32 v[152:153], v[240:241], s[12:13], v[152:153] op_sel_hi:[1,0,1]
	global_store_dwordx4 v[198:199], v[152:155], off offset:1024
	v_pk_mul_f32 v[246:247], v[28:29], v[246:247]
	v_pk_mul_f32 v[244:245], v[26:27], v[244:245]
	v_pk_fma_f32 v[158:159], v[246:247], s[12:13], v[158:159] op_sel_hi:[1,0,1]
	v_pk_fma_f32 v[156:157], v[244:245], s[12:13], v[156:157] op_sel_hi:[1,0,1]
	global_store_dwordx4 v[198:199], v[156:159], off offset:2048
	v_pk_mul_f32 v[250:251], v[32:33], v[250:251]
	v_pk_mul_f32 v[248:249], v[30:31], v[248:249]
	v_pk_fma_f32 v[162:163], v[250:251], s[12:13], v[162:163] op_sel_hi:[1,0,1]
	v_pk_fma_f32 v[160:161], v[248:249], s[12:13], v[160:161] op_sel_hi:[1,0,1]
	global_store_dwordx4 v[198:199], v[160:163], off offset:3072

; __device__ __forceinline__ f32x4 unpack_f8x4(unsigned w) { const auto lo = __builtin_amdgcn_cvt_pk_f32_fp8((int)w, false), hi = __builtin_amdgcn_cvt_pk_f32_fp8((int)w, true); return (f32x4){lo[0], lo[1], hi[0], hi[1]}; }
; __device__ __forceinline__ void gather_y(const Ctx& F, const int s, f32x4 (&acc)[8]) {
; #pragma unroll
;     for (int j = 0; j < 8; ++j) acc[j] = (f32x4){0.f, 0.f, 0.f, 0.f};
;     unsigned m = (unsigned)__ballot(s >= 0) & 0xffffu;
;     while (m) {
;         const int e0 = __builtin_ctz(m); m &= m - 1;
;         const bool two = m != 0; const int e1 = two ? __builtin_ctz(m) : e0; if (two) m &= m - 1;
;         const int s0 = __builtin_amdgcn_readlane(s, e0), s1 = __builtin_amdgcn_readlane(s, e1);
;         const unsigned char* y0 = F.y8 + (size_t)s0 * DM + 4 * F.lane; const unsigned char* y1 = F.y8 + (size_t)s1 * DM + 4 * F.lane;
;         unsigned w0[8], w1[8];
; #pragma unroll
;         for (int j = 0; j < 8; ++j) w0[j] = __builtin_nontemporal_load((const unsigned*)(y0 + 256 * j));
; #pragma unroll
;         for (int j = 0; j < 8; ++j) w1[j] = __builtin_nontemporal_load((const unsigned*)(y1 + 256 * j));
;         const float k1 = two ? 1.f : 0.f;
; #pragma unroll
;         for (int j = 0; j < 8; ++j) { acc[j] += unpack_f8x4(w0[j]); acc[j] += unpack_f8x4(w1[j]) * k1; }
;     }
; }
; __device__ __forceinline__ void phase_norm1(const Params& p, const Ctx& F, const int l) {
;     ...
;         { const int t2 = t + tstride;
;           if (t2 < TPB) { const float* xs2; float* xd2; row_ptrs(p, F, l, b, t2, xs2, xd2);
; #pragma unroll
;             for (int j = 0; j < 8; ++j) vn[j] = __builtin_nontemporal_load((const f32x4*)xs2 + F.lane + 64 * j);
;             if (comb) {
; #pragma unroll
;                 for (int j = 0; j < 8; ++j) dn[j] = __builtin_nontemporal_load((const u32x2*)(F.dlt + ((size_t)b * TPB + t2) * DM + 4 * F.lane + 256 * j)); }
;             if (comb) { { if (fin) gather_y1(F, sn, accn); else gather_y(F, sn, accn); } const int t3 = t2 + tstride; sn = -1; if (t3 < TPB && F.lane < 16) sn = F.slot[(unsigned)((b * 16 + F.lane) * TPB + t3)]; } } }
.LBB0_164:
	s_lshl_b64 s[14:15], s[14:15], 13
	s_add_u32 s12, s12, s14
	s_addc_u32 s13, s13, s15
	v_lshl_add_u64 v[52:53], s[12:13], 0, v[34:35]
	v_add_co_u32_e32 v64, vcc, 0x1000, v52
	global_load_dwordx4 v[36:39], v34, s[12:13] nt
	global_load_dwordx4 v[40:43], v34, s[12:13] offset:1024 nt
	global_load_dwordx4 v[44:47], v34, s[12:13] offset:2048 nt
	global_load_dwordx4 v[48:51], v34, s[12:13] offset:3072 nt
	v_addc_co_u32_e32 v65, vcc, 0, v53, vcc
	global_load_dwordx4 v[52:55], v[64:65], off nt
	global_load_dwordx4 v[56:59], v[64:65], off offset:1024 nt
	global_load_dwordx4 v[60:63], v[64:65], off offset:2048 nt
	s_nop 0
	global_load_dwordx4 v[64:67], v[64:65], off offset:3072 nt
	s_and_b64 vcc, exec, s[0:1]
	s_cbranch_vccnz .LBB0_172
	s_ashr_i32 s1, s31, 31
	s_add_u32 s0, s21, s31
	s_addc_u32 s1, 0, s1
	s_lshl_b64 s[0:1], s[0:1], 12
	v_lshl_add_u64 v[2:3], v[182:183], 0, s[0:1]
	global_load_dwordx2 v[164:165], v[2:3], off nt
	global_load_dwordx2 v[166:167], v[2:3], off offset:512 nt
	global_load_dwordx2 v[168:169], v[2:3], off offset:1024 nt
	global_load_dwordx2 v[170:171], v[2:3], off offset:1536 nt
	global_load_dwordx2 v[172:173], v[2:3], off offset:2048 nt
	global_load_dwordx2 v[176:177], v[2:3], off offset:2560 nt
	global_load_dwordx2 v[178:179], v[2:3], off offset:3072 nt
	global_load_dwordx2 v[174:175], v[2:3], off offset:3584 nt
	v_cmp_lt_i32_e32 vcc, -1, v202
	s_and_b32 s56, vcc_lo, 0xffff
	v_mov_b32_e32 v2, v35
	v_mov_b32_e32 v3, v35
	v_mov_b32_e32 v4, v35
	v_mov_b32_e32 v5, v35
	v_mov_b32_e32 v6, v35
	v_mov_b32_e32 v7, v35
	v_mov_b32_e32 v8, v35
	v_mov_b32_e32 v9, v35
	v_mov_b32_e32 v10, v35
	v_mov_b32_e32 v11, v35
	v_mov_b32_e32 v12, v35
	v_mov_b32_e32 v13, v35
	v_mov_b32_e32 v14, v35
	v_mov_b32_e32 v15, v35
	v_mov_b32_e32 v16, v35
	v_mov_b32_e32 v17, v35
	v_mov_b32_e32 v18, v35
	v_mov_b32_e32 v19, v35
	v_mov_b32_e32 v20, v35
	v_mov_b32_e32 v21, v35
	v_mov_b32_e32 v22, v35
	v_mov_b32_e32 v23, v35
	v_mov_b32_e32 v24, v35
	v_mov_b32_e32 v25, v35
	v_mov_b32_e32 v26, v35
	v_mov_b32_e32 v27, v35
	v_mov_b32_e32 v28, v35
	v_mov_b32_e32 v29, v35
	v_mov_b32_e32 v30, v35
	v_mov_b32_e32 v31, v35
	v_mov_b32_e32 v32, v35
	v_mov_b32_e32 v33, v35
	s_mov_b32 s57, 1
	s_cmp_eq_u32 s56, 0
	s_cbranch_scc1 .Lgs_noexp
	s_mov_b32 s57, 2
	s_add_i32 s1, s56, -1
	s_and_b32 s12, s1, s56
	s_ff1_i32_b32 s13, s56
	v_sub_co_u32_e64 v210, s[0:1], s12, 1
	s_ff1_i32_b32 s16, s12
	s_and_b64 s[14:15], s[0:1], exec
	s_cselect_b32 s15, s13, s16
	s_cselect_b32 s58, 0, 1.0
	v_readlane_b32 s14, v202, s13
	v_readlane_b32 s16, v202, s15
	s_ashr_i32 s15, s14, 31
	s_lshl_b64 s[14:15], s[14:15], 11
	s_ashr_i32 s17, s16, 31
	v_lshl_add_u64 v[250:251], v[184:185], 0, s[14:15]
	s_lshl_b64 s[14:15], s[16:17], 11
	global_load_dword v234, v[250:251], off nt
	global_load_dword v235, v[250:251], off offset:256 nt
	global_load_dword v236, v[250:251], off offset:512 nt
	global_load_dword v237, v[250:251], off offset:768 nt
	global_load_dword v238, v[250:251], off offset:1024 nt
	global_load_dword v239, v[250:251], off offset:1280 nt
	global_load_dword v240, v[250:251], off offset:1536 nt
	global_load_dword v241, v[250:251], off offset:1792 nt
	v_lshl_add_u64 v[250:251], v[184:185], 0, s[14:15]
	global_load_dword v242, v[250:251], off nt
	global_load_dword v243, v[250:251], off offset:256 nt
	global_load_dword v244, v[250:251], off offset:512 nt
	global_load_dword v245, v[250:251], off offset:768 nt
	global_load_dword v246, v[250:251], off offset:1024 nt
	global_load_dword v247, v[250:251], off offset:1280 nt
	global_load_dword v248, v[250:251], off offset:1536 nt
	global_load_dword v249, v[250:251], off offset:1792 nt
	v_readfirstlane_b32 s0, v210
	s_and_b32 s56, s0, s12
.Lgs_noexp:
	s_add_i32 s12, s31, s18
	s_cmpk_lt_i32 s12, 0x1100
	s_cselect_b64 s[0:1], -1, 0
	s_and_b64 s[14:15], s[0:1], s[4:5]
	v_mov_b32_e32 v251, -1
	s_and_saveexec_b64 s[0:1], s[14:15]
	s_cbranch_execz .Lgs_sn_done
	v_add_u32_e32 v198, s12, v209
	v_mov_b32_e32 v199, v35
	v_lshl_add_u64 v[198:199], v[198:199], 2, s[8:9]
	global_load_dword v251, v[198:199], off
